# attention K/V staging: counted vmcnt(7..4) before SWRITE in steady state (younger slot loads stay in flight; restores 2-tile prefetch distance), vmcnt(3..0) only on last iterations
# baseline (speedup 1.0000x reference)
.LBB0_712:
	s_add_i32 s27, s26, 2
	s_cmp_ge_u32 s27, s22
	s_cbranch_scc1 .Lsw0a_last
	s_waitcnt vmcnt(7)
	ds_write_b128 v229, v[146:149] offset:16384
	s_waitcnt vmcnt(6)
	ds_write_b128 v230, v[150:153] offset:16384
	s_waitcnt vmcnt(5)
	ds_write_b128 v231, v[158:161] offset:49152
	s_waitcnt vmcnt(4)
	ds_write_b128 v232, v[166:169] offset:49152
	s_branch .Lsw0a_done

.Lsw0a_done:
	s_waitcnt lgkmcnt(0)
	s_cmp_gt_u32 s26, s20
	s_barrier
	s_cbranch_scc1 .LBB0_714
	s_lshl_b64 s[28:29], s[6:7], 6
	v_mov_b32_e32 v5, s29
	v_or_b32_e32 v4, s28, v193
	v_lshlrev_b64 v[4:5], 11, v[4:5]
	v_mov_b32_e32 v9, s29
	v_or_b32_e32 v8, s28, v194
	v_lshl_add_u64 v[6:7], v[186:187], 0, v[4:5]
	v_lshlrev_b64 v[8:9], 11, v[8:9]
	v_lshl_add_u64 v[4:5], v[188:189], 0, v[4:5]
	v_lshl_add_u64 v[10:11], v[186:187], 0, v[8:9]
	global_load_dwordx4 v[146:149], v[6:7], off
	global_load_dwordx4 v[150:153], v[10:11], off
	v_lshl_add_u64 v[6:7], v[188:189], 0, v[8:9]
	global_load_dwordx4 v[158:161], v[4:5], off
	global_load_dwordx4 v[166:169], v[6:7], off

.LBB0_718:
	s_add_i32 s27, s26, 2
	s_cmp_ge_u32 s27, s22
	s_cselect_b64 s[28:29], -1, 0
	s_and_b64 vcc, exec, s[28:29]
	s_cbranch_vccnz .LBB0_720
	s_cmp_gt_u32 s26, s20
	s_cbranch_scc1 .Lsw0b_last
	s_waitcnt vmcnt(7)
	ds_write_b128 v229, v[154:157]
	s_waitcnt vmcnt(6)
	ds_write_b128 v230, v[162:165]
	s_waitcnt vmcnt(5)
	ds_write_b128 v231, v[170:173] offset:32768
	s_waitcnt vmcnt(4)
	ds_write_b128 v232, v[174:177] offset:32768
	s_branch .LBB0_720
.Lsw0b_last:
	s_waitcnt vmcnt(3)
	ds_write_b128 v229, v[154:157]
	s_waitcnt vmcnt(2)
	ds_write_b128 v230, v[162:165]
	s_waitcnt vmcnt(1)
	ds_write_b128 v231, v[170:173] offset:32768
	s_waitcnt vmcnt(0)
	ds_write_b128 v232, v[174:177] offset:32768

.LBB0_2280:
	s_add_i32 s34, s33, 2
	s_cmp_ge_u32 s34, s28
	s_cbranch_scc1 .Lsw1a_last
	s_waitcnt vmcnt(7)
	ds_write_b128 v229, v[146:149] offset:16384
	s_waitcnt vmcnt(6)
	ds_write_b128 v230, v[150:153] offset:16384
	s_waitcnt vmcnt(5)
	ds_write_b128 v231, v[158:161] offset:49152
	s_waitcnt vmcnt(4)
	ds_write_b128 v232, v[166:169] offset:49152
	s_branch .Lsw1a_done

.Lsw1a_done:
	s_waitcnt lgkmcnt(0)
	s_cmp_gt_u32 s33, s24
	s_barrier
	s_cbranch_scc1 .LBB0_2282
	s_lshl_b64 s[26:27], s[6:7], 6
	v_mov_b32_e32 v5, s27
	v_or_b32_e32 v4, s26, v193
	v_lshlrev_b64 v[4:5], 11, v[4:5]
	v_mov_b32_e32 v9, s27
	v_or_b32_e32 v8, s26, v194
	v_lshl_add_u64 v[6:7], v[186:187], 0, v[4:5]
	v_lshlrev_b64 v[8:9], 11, v[8:9]
	v_lshl_add_u64 v[4:5], v[188:189], 0, v[4:5]
	v_lshl_add_u64 v[10:11], v[186:187], 0, v[8:9]
	global_load_dwordx4 v[146:149], v[6:7], off
	global_load_dwordx4 v[150:153], v[10:11], off
	v_lshl_add_u64 v[6:7], v[188:189], 0, v[8:9]
	global_load_dwordx4 v[158:161], v[4:5], off
	global_load_dwordx4 v[166:169], v[6:7], off

.LBB0_2286:
	s_add_i32 s34, s33, 2
	s_cmp_ge_u32 s34, s28
	s_cselect_b64 s[26:27], -1, 0
	s_and_b64 vcc, exec, s[26:27]
	s_cbranch_vccnz .LBB0_2288
	s_cmp_gt_u32 s33, s24
	s_cbranch_scc1 .Lsw1b_last
	s_waitcnt vmcnt(7)
	ds_write_b128 v229, v[154:157]
	s_waitcnt vmcnt(6)
	ds_write_b128 v230, v[162:165]
	s_waitcnt vmcnt(5)
	ds_write_b128 v231, v[170:173] offset:32768
	s_waitcnt vmcnt(4)
	ds_write_b128 v232, v[174:177] offset:32768
	s_branch .LBB0_2288
